# stack F1 + key-loop back edge rotated: closing barrier is the loop head, exit test + taken back-branch execute before it, exit path has its own barrier copy
# speedup vs baseline: 1.0093x; 1.0093x over previous
.LBB0_757:
	s_barrier
	s_add_i32 s6, 0, 0x12000
	v_add_u32_e32 v199, s6, v170
	v_add_u32_e32 v204, s6, v171
	v_add_u32_e32 v205, s6, v172
	ds_read_b128 v[64:67], v180 offset:49152
	ds_read_b128 v[68:71], v180 offset:57344
	ds_read_b128 v[200:203], v181 offset:49152
	ds_read_b128 v[226:229], v181 offset:57344
	ds_read_b128 v[230:233], v182 offset:49152
	ds_read_b128 v[234:237], v182 offset:57344
	ds_read_b128 v[238:241], v183 offset:49152
	ds_read_b128 v[242:245], v183 offset:57344
	s_waitcnt lgkmcnt(7)
	v_mfma_f32_32x32x16_bf16 v[80:95], v[64:67], v[124:127], 0
	s_add_i32 s12, s64, -1
	s_sub_i32 s80, s11, 64
	s_cmp_lt_u32 s12, 3
	s_cselect_b32 s80, s10, s80
	s_mul_i32 s81, s80, 0xc00
	s_add_i32 s85, s82, 0x8000
	s_mov_b32 m0, s85
	s_add_i32 s85, s82, 0x10000
	buffer_load_dwordx4 v154, s[72:75], s81 offen lds
	v_exp_f32_e32 v216, v128
	v_add_f32_e32 v128, 0, v222
	v_add_f32_e32 v128, v224, v128
	v_add_f32_e32 v128, v220, v128
	v_add_f32_e32 v128, v223, v128
	v_add_f32_e32 v128, v219, v128
	v_add_f32_e32 v128, v221, v128
	s_waitcnt lgkmcnt(6)
	v_mfma_f32_32x32x16_bf16 v[64:79], v[68:71], v[124:127], 0
	s_mov_b32 m0, s85
	s_add_i32 s85, s82, 0xa000
	buffer_load_dwordx4 v155, s[72:75], s81 offen lds
	v_add_f32_e32 v128, v217, v128
	v_add_f32_e32 v128, v218, v128
	v_add_f32_e32 v128, v212, v128
	v_add_f32_e32 v128, v214, v128
	v_add_f32_e32 v128, v211, v128
	v_add_f32_e32 v128, v213, v128
	v_exp_f32_e32 v138, v138
	s_waitcnt lgkmcnt(5)
	v_mfma_f32_32x32x16_bf16 v[80:95], v[200:203], v[120:123], v[80:95]
	s_mov_b32 m0, s85
	s_add_i32 s81, s81, 0x18000
	buffer_load_dwordx4 v154, s[72:75], s81 offen lds
	v_add_f32_e32 v128, v208, v128
	v_exp_f32_e32 v139, v139
	v_add_f32_e32 v128, v210, v128
	v_exp_f32_e32 v164, v136
	v_add_f32_e32 v128, v207, v128
	v_exp_f32_e32 v137, v137
	v_add_f32_e32 v128, v209, v128
	s_waitcnt lgkmcnt(4)
	v_mfma_f32_32x32x16_bf16 v[64:79], v[226:229], v[120:123], v[64:79]
	s_lshl_b32 s81, s83, 11
	s_add_i32 s85, s82, 0x4000
	s_mov_b32 m0, s85
	s_add_i32 s85, s82, 0x6000
	buffer_load_dwordx4 v158, s[76:79], s81 offen lds
	ds_read_b128 v[200:203], v184 offset:49152
	ds_read_b128 v[226:229], v184 offset:57344
	v_exp_f32_e32 v165, v132
	v_add_f32_e32 v128, v138, v128
	v_add_f32_e32 v128, v139, v128
	v_exp_f32_e32 v206, v130
	v_add_f32_e32 v128, v164, v128
	v_exp_f32_e32 v215, v131
	s_waitcnt lgkmcnt(5)
	v_mfma_f32_32x32x16_bf16 v[80:95], v[230:233], v[116:119], v[80:95]
	s_mov_b32 m0, s85
	s_add_i32 s81, s81, 0x10000
	buffer_load_dwordx4 v158, s[76:79], s81 offen lds
	s_mov_b32 s84, s80
	v_add_f32_e32 v128, v137, v128
	v_add_f32_e32 v128, v165, v128
	v_exp_f32_e32 v225, v129
	v_exp_f32_e32 v162, v162
	v_exp_f32_e32 v163, v163
	v_exp_f32_e32 v160, v160
	v_exp_f32_e32 v161, v161
	s_waitcnt lgkmcnt(4)
	v_mfma_f32_32x32x16_bf16 v[64:79], v[234:237], v[116:119], v[64:79]
	ds_read_b128 v[230:233], v185 offset:49152
	ds_read_b128 v[234:237], v185 offset:57344
	v_cvt_pk_bf16_f32 v129, v220, v223
	v_cvt_pk_bf16_f32 v130, v219, v221
	v_cvt_pk_bf16_f32 v131, v217, v218
	v_cvt_pk_bf16_f32 v132, v212, v214
	v_cvt_pk_bf16_f32 v136, v138, v139
	v_cvt_pk_bf16_f32 v137, v164, v137
	s_waitcnt lgkmcnt(5)
	v_mfma_f32_32x32x16_bf16 v[80:95], v[238:241], v[112:115], v[80:95]
	v_cvt_pk_bf16_f32 v139, v206, v215
	v_permlane32_swap_b32_e32 v129, v131
	s_nop 0
	v_permlane32_swap_b32_e32 v137, v139
	s_waitcnt lgkmcnt(4)
	v_mfma_f32_32x32x16_bf16 v[64:79], v[242:245], v[112:115], v[64:79]
	ds_read_b128 v[238:241], v186 offset:49152
	ds_read_b128 v[242:245], v186 offset:57344
	s_waitcnt lgkmcnt(5)
	v_mfma_f32_32x32x16_bf16 v[80:95], v[200:203], v[108:111], v[80:95]
	s_waitcnt lgkmcnt(4)
	v_mfma_f32_32x32x16_bf16 v[64:79], v[226:229], v[108:111], v[64:79]
	ds_read_b128 v[200:203], v187 offset:49152
	ds_read_b128 v[226:229], v187 offset:57344
	s_waitcnt lgkmcnt(5)
	v_mfma_f32_32x32x16_bf16 v[80:95], v[230:233], v[104:107], v[80:95]
	s_waitcnt lgkmcnt(4)
	v_mfma_f32_32x32x16_bf16 v[64:79], v[234:237], v[104:107], v[64:79]
	ds_read_b128 v[230:233], v199
	ds_read_b128 v[234:237], v199 offset:4096
	ds_read_b128 v[246:249], v190
	s_waitcnt lgkmcnt(6)
	v_mfma_f32_32x32x16_bf16 v[80:95], v[238:241], v[100:103], v[80:95]
	s_waitcnt lgkmcnt(5)
	v_mfma_f32_32x32x16_bf16 v[64:79], v[242:245], v[100:103], v[64:79]
	ds_read_b128 v[238:241], v204
	ds_read_b128 v[242:245], v204 offset:4096
	ds_read_b128 v[250:253], v190 offset:1024
	v_add_u32_e32 v204, s6, v173
	s_waitcnt lgkmcnt(7)
	v_mfma_f32_32x32x16_bf16 v[80:95], v[200:203], v[96:99], v[80:95]
	s_waitcnt lgkmcnt(6)
	v_mfma_f32_32x32x16_bf16 v[64:79], v[226:229], v[96:99], v[64:79]
	ds_read_b128 v[200:203], v205
	ds_read_b128 v[226:229], v205 offset:4096
	s_waitcnt lgkmcnt(5)
	v_mfma_f32_32x32x16_bf16 v[80:95], v[230:233], v[246:249], v[80:95]
	s_waitcnt lgkmcnt(5)
	v_mfma_f32_32x32x16_bf16 v[64:79], v[234:237], v[246:249], v[64:79]
	ds_read_b128 v[230:233], v204
	ds_read_b128 v[234:237], v204 offset:4096
	ds_read_b128 v[246:249], v190 offset:2048
	s_waitcnt lgkmcnt(5)
	v_mfma_f32_32x32x16_bf16 v[80:95], v[238:241], v[250:253], v[80:95]
	s_waitcnt lgkmcnt(5)
	v_mfma_f32_32x32x16_bf16 v[64:79], v[242:245], v[250:253], v[64:79]
	ds_read_b128 v[250:253], v190 offset:3072
	s_waitcnt lgkmcnt(1)
	v_mfma_f32_32x32x16_bf16 v[80:95], v[200:203], v[246:249], v[80:95]
	v_exp_f32_e32 v205, v133
	v_cvt_pk_bf16_f32 v133, v211, v213
	v_cvt_pk_bf16_f32 v138, v165, v205
	v_add_f32_e32 v128, v205, v128
	v_add_f32_e32 v128, v206, v128
	v_add_f32_e32 v128, v215, v128
	s_waitcnt lgkmcnt(1)
	v_mfma_f32_32x32x16_bf16 v[64:79], v[226:229], v[246:249], v[64:79]
	v_add_f32_e32 v128, v216, v128
	v_add_f32_e32 v128, v225, v128
	v_add_f32_e32 v128, v162, v128
	v_add_f32_e32 v128, v163, v128
	v_add_f32_e32 v128, v160, v128
	v_add_f32_e32 v128, v161, v128
	s_waitcnt lgkmcnt(0)
	v_mfma_f32_32x32x16_bf16 v[80:95], v[230:233], v[250:253], v[80:95]
	v_exp_f32_e32 v226, v134
	v_exp_f32_e32 v227, v135
	v_cvt_pk_bf16_f32 v134, v208, v210
	v_cvt_pk_bf16_f32 v135, v207, v209
	v_add_f32_e32 v128, v226, v128
	v_add_f32_e32 v203, v227, v128
	v_mov_b32_e32 v204, v203
	s_waitcnt lgkmcnt(0)
	v_mfma_f32_32x32x16_bf16 v[64:79], v[234:237], v[250:253], v[64:79]
	s_nop 0
	v_permlane32_swap_b32_e32 v203, v204
	v_cvt_pk_bf16_f32 v128, v222, v224
	v_cvt_pk_bf16_f32 v208, v216, v225
	v_cvt_pk_bf16_f32 v209, v162, v163
	v_cvt_pk_bf16_f32 v210, v160, v161
	v_cvt_pk_bf16_f32 v211, v226, v227
	v_permlane32_swap_b32_e32 v132, v134
	v_permlane32_swap_b32_e32 v128, v130
	v_permlane32_swap_b32_e32 v133, v135
	v_permlane32_swap_b32_e32 v136, v138
	v_permlane32_swap_b32_e32 v208, v210
	v_permlane32_swap_b32_e32 v209, v211
	ds_read_b64_tr_b16 v[160:161], v167 offset:0
	ds_read_b64_tr_b16 v[162:163], v167 offset:0x800
	ds_read_b64_tr_b16 v[232:233], v167 offset:0x1000
	ds_read_b64_tr_b16 v[234:235], v167 offset:0x1800
	ds_read_b64_tr_b16 v[236:237], v167 offset:0x2000
	ds_read_b64_tr_b16 v[238:239], v167 offset:0x2800
	ds_read_b64_tr_b16 v[240:241], v167 offset:0x3000
	ds_read_b64_tr_b16 v[242:243], v167 offset:0x3800
	v_max_f32_e32 v164, v81, v81
	v_max_f32_e32 v165, v80, v80
	v_max_f32_e32 v164, v165, v164
	v_max3_f32 v164, v164, v82, v83
	v_max3_f32 v164, v164, v84, v85
	v_max3_f32 v164, v164, v86, v87
	v_max3_f32 v164, v164, v88, v89
	v_max3_f32 v164, v164, v90, v91
	v_max3_f32 v164, v164, v92, v93
	v_max3_f32 v164, v164, v94, v95
	s_waitcnt lgkmcnt(0)
	v_mfma_f32_32x32x16_bf16 v[16:31], v[128:131], v[160:163], v[16:31]
	v_max3_f32 v160, v164, v64, v65
	v_max3_f32 v160, v160, v66, v67
	v_max3_f32 v160, v160, v68, v69
	v_mfma_f32_32x32x16_bf16 v[16:31], v[132:135], v[232:235], v[16:31]
	ds_read_b64_tr_b16 v[232:233], v167 offset:0x200
	ds_read_b64_tr_b16 v[234:235], v167 offset:0xa00
	v_max3_f32 v160, v160, v70, v71
	v_max3_f32 v160, v160, v72, v73
	v_max3_f32 v160, v160, v74, v75
	v_mfma_f32_32x32x16_bf16 v[16:31], v[136:139], v[236:239], v[16:31]
	ds_read_b64_tr_b16 v[236:237], v167 offset:0x1200
	ds_read_b64_tr_b16 v[238:239], v167 offset:0x1a00
	ds_read_b64_tr_b16 v[244:245], v167 offset:0x2200
	ds_read_b64_tr_b16 v[246:247], v167 offset:0x2a00
	ds_read_b64_tr_b16 v[248:249], v167 offset:0x3200
	ds_read_b64_tr_b16 v[250:251], v167 offset:0x3a00
	v_max3_f32 v160, v160, v76, v77
	v_max3_f32 v160, v160, v78, v79
	v_mov_b32_e32 v161, v160
	v_mfma_f32_32x32x16_bf16 v[16:31], v[208:211], v[240:243], v[16:31]
	v_max_f32_e32 v162, v198, v198
	v_permlane32_swap_b32_e32 v160, v161
	v_max_f32_e32 v161, v161, v161
	v_max_f32_e32 v160, v160, v160
	v_max_f32_e32 v160, v160, v161
	s_waitcnt lgkmcnt(0)
	v_mfma_f32_32x32x16_bf16 v[32:47], v[128:131], v[232:235], v[32:47]
	ds_read_b64_tr_b16 v[232:233], v167 offset:0x400
	ds_read_b64_tr_b16 v[234:235], v167 offset:0xc00
	v_sub_f32_e32 v161, v160, v198
	v_max_f32_e32 v160, v162, v160
	v_sub_f32_e32 v162, v198, v160
	v_mul_f32_e32 v162, 0x3dd53b94, v162
	v_exp_f32_e32 v162, v162
	v_mfma_f32_32x32x16_bf16 v[32:47], v[132:135], v[236:239], v[32:47]
	ds_read_b64_tr_b16 v[236:237], v167 offset:0x1400
	ds_read_b64_tr_b16 v[238:239], v167 offset:0x1c00
	ds_read_b64_tr_b16 v[240:241], v167 offset:0x2400
	ds_read_b64_tr_b16 v[242:243], v167 offset:0x2c00
	v_cmp_ge_f32_e32 vcc, s48, v161
	s_cmp_eq_u64 vcc, exec
	s_cselect_b64 s[6:7], -1, 0
	v_cndmask_b32_e64 v206, v162, 1.0, s[6:7]
	v_cndmask_b32_e64 v160, v160, v198, s[6:7]
	v_mul_f32_e32 v205, 0xbdd53b94, v160
	v_cmp_gt_f32_e32 vcc, 1.0, v206
	v_mfma_f32_32x32x16_bf16 v[32:47], v[136:139], v[244:247], v[32:47]
	ds_read_b64_tr_b16 v[244:245], v167 offset:0x3400
	ds_read_b64_tr_b16 v[246:247], v167 offset:0x3c00
	v_fmamk_f32 v87, v87, 0x3dd53b94, v205
	v_fmamk_f32 v80, v80, 0x3dd53b94, v205
	v_fmamk_f32 v81, v81, 0x3dd53b94, v205
	v_fmamk_f32 v82, v82, 0x3dd53b94, v205
	v_fmamk_f32 v83, v83, 0x3dd53b94, v205
	v_mfma_f32_32x32x16_bf16 v[32:47], v[208:211], v[248:251], v[32:47]
	v_fmamk_f32 v84, v84, 0x3dd53b94, v205
	v_fmamk_f32 v85, v85, 0x3dd53b94, v205
	v_fmamk_f32 v86, v86, 0x3dd53b94, v205
	v_fmamk_f32 v88, v88, 0x3dd53b94, v205
	v_fmamk_f32 v89, v89, 0x3dd53b94, v205
	s_waitcnt lgkmcnt(0)
	v_mfma_f32_32x32x16_bf16 v[0:15], v[128:131], v[232:235], v[0:15]
	ds_read_b64_tr_b16 v[232:233], v167 offset:0x600
	ds_read_b64_tr_b16 v[234:235], v167 offset:0xe00
	v_fmamk_f32 v90, v90, 0x3dd53b94, v205
	v_fmamk_f32 v91, v91, 0x3dd53b94, v205
	v_fmamk_f32 v92, v92, 0x3dd53b94, v205
	v_fmamk_f32 v93, v93, 0x3dd53b94, v205
	v_fmamk_f32 v94, v94, 0x3dd53b94, v205
	v_mfma_f32_32x32x16_bf16 v[0:15], v[132:135], v[236:239], v[0:15]
	ds_read_b64_tr_b16 v[236:237], v167 offset:0x1600
	ds_read_b64_tr_b16 v[238:239], v167 offset:0x1e00
	v_fmamk_f32 v95, v95, 0x3dd53b94, v205
	v_fmamk_f32 v215, v64, 0x3dd53b94, v205
	v_fmamk_f32 v216, v65, 0x3dd53b94, v205
	v_fmamk_f32 v217, v66, 0x3dd53b94, v205
	v_fmamk_f32 v218, v67, 0x3dd53b94, v205
	v_mfma_f32_32x32x16_bf16 v[0:15], v[136:139], v[240:243], v[0:15]
	ds_read_b64_tr_b16 v[240:241], v167 offset:0x2600
	ds_read_b64_tr_b16 v[242:243], v167 offset:0x2e00
	ds_read_b64_tr_b16 v[248:249], v167 offset:0x3600
	ds_read_b64_tr_b16 v[250:251], v167 offset:0x3e00
	v_fmamk_f32 v219, v68, 0x3dd53b94, v205
	v_fmamk_f32 v212, v73, 0x3dd53b94, v205
	v_fmamk_f32 v213, v74, 0x3dd53b94, v205
	v_fmamk_f32 v214, v75, 0x3dd53b94, v205
	v_mfma_f32_32x32x16_bf16 v[0:15], v[208:211], v[244:247], v[0:15]
	v_fmamk_f32 v207, v76, 0x3dd53b94, v205
	v_fmamk_f32 v220, v77, 0x3dd53b94, v205
	v_fmamk_f32 v221, v78, 0x3dd53b94, v205
	s_waitcnt lgkmcnt(0)
	v_mfma_f32_32x32x16_bf16 v[48:63], v[128:131], v[232:235], v[48:63]
	v_exp_f32_e32 v128, v80
	v_exp_f32_e32 v129, v82
	v_exp_f32_e32 v130, v84
	v_exp_f32_e32 v131, v86
	v_mfma_f32_32x32x16_bf16 v[48:63], v[132:135], v[236:239], v[48:63]
	v_exp_f32_e32 v132, v88
	v_exp_f32_e32 v133, v90
	v_exp_f32_e32 v134, v92
	v_exp_f32_e32 v135, v94
	v_mfma_f32_32x32x16_bf16 v[48:63], v[136:139], v[240:243], v[48:63]
	v_exp_f32_e32 v139, v89
	v_exp_f32_e32 v138, v91
	v_exp_f32_e32 v137, v93
	v_exp_f32_e32 v136, v95
	v_mfma_f32_32x32x16_bf16 v[48:63], v[208:211], v[248:251], v[48:63]
	v_exp_f32_e32 v161, v87
	v_exp_f32_e32 v198, v81
	v_exp_f32_e32 v163, v83
	v_exp_f32_e32 v162, v85
	v_fmamk_f32 v208, v69, 0x3dd53b94, v205
	v_fmamk_f32 v209, v70, 0x3dd53b94, v205
	v_fmamk_f32 v210, v71, 0x3dd53b94, v205
	v_fmamk_f32 v211, v72, 0x3dd53b94, v205
	v_fmac_f32_e32 v205, 0x3dd53b94, v79
	s_cbranch_vccz .LBB0_761
	s_and_saveexec_b64 s[8:9], s[4:5]
	ds_write_b32 v189, v206 offset:128
	s_or_b64 exec, exec, s[8:9]
	s_waitcnt lgkmcnt(0)
	v_add_u32_e32 v248, s62, v169
	ds_read_b128 v[232:235], v248 offset:224
	ds_read_b128 v[236:239], v248 offset:192
	ds_read_b128 v[240:243], v248 offset:160
	ds_read_b128 v[244:247], v248 offset:128
	s_waitcnt lgkmcnt(3)
	v_pk_mul_f32 v[28:29], v[28:29], v[232:233]
	s_waitcnt lgkmcnt(2)
	v_pk_mul_f32 v[24:25], v[24:25], v[236:237]
	s_waitcnt lgkmcnt(1)
	v_pk_mul_f32 v[20:21], v[20:21], v[240:241]
	v_pk_mul_f32 v[30:31], v[30:31], v[234:235]
	v_pk_mul_f32 v[26:27], v[26:27], v[238:239]
	v_pk_mul_f32 v[22:23], v[22:23], v[242:243]
	s_waitcnt lgkmcnt(0)
	v_pk_mul_f32 v[18:19], v[18:19], v[246:247]
	v_pk_mul_f32 v[16:17], v[16:17], v[244:245]
	v_pk_mul_f32 v[44:45], v[44:45], v[232:233]
	v_pk_mul_f32 v[40:41], v[40:41], v[236:237]
	v_pk_mul_f32 v[36:37], v[36:37], v[240:241]
	v_pk_mul_f32 v[46:47], v[46:47], v[234:235]
	v_pk_mul_f32 v[42:43], v[42:43], v[238:239]
	v_pk_mul_f32 v[38:39], v[38:39], v[242:243]
	v_pk_mul_f32 v[34:35], v[34:35], v[246:247]
	v_pk_mul_f32 v[32:33], v[32:33], v[244:245]
	v_pk_mul_f32 v[12:13], v[12:13], v[232:233]
	v_pk_mul_f32 v[8:9], v[8:9], v[236:237]
	v_pk_mul_f32 v[4:5], v[4:5], v[240:241]
	v_pk_mul_f32 v[14:15], v[14:15], v[234:235]
	v_pk_mul_f32 v[10:11], v[10:11], v[238:239]
	v_pk_mul_f32 v[6:7], v[6:7], v[242:243]
	v_pk_mul_f32 v[2:3], v[2:3], v[246:247]
	v_pk_mul_f32 v[0:1], v[0:1], v[244:245]
	v_pk_mul_f32 v[60:61], v[60:61], v[232:233]
	v_pk_mul_f32 v[56:57], v[56:57], v[236:237]
	v_pk_mul_f32 v[52:53], v[52:53], v[240:241]
	v_pk_mul_f32 v[62:63], v[62:63], v[234:235]
	v_pk_mul_f32 v[58:59], v[58:59], v[238:239]
	v_pk_mul_f32 v[54:55], v[54:55], v[242:243]
	v_pk_mul_f32 v[50:51], v[50:51], v[246:247]
	v_pk_mul_f32 v[48:49], v[48:49], v[244:245]

.LBB0_765:
	s_cmp_ge_u32 s64, s63
	s_waitcnt vmcnt(0) lgkmcnt(0)
	s_cbranch_scc1 .Lattn_exit_1
	v_mov_b32_e32 v197, v205
	s_branch .LBB0_757
.Lattn_exit_1:
	s_barrier

.LBB0_2012:
	s_barrier
	s_add_i32 s6, 0, 0x12000
	v_add_u32_e32 v199, s6, v170
	v_add_u32_e32 v204, s6, v171
	v_add_u32_e32 v205, s6, v172
	ds_read_b128 v[64:67], v180 offset:49152
	ds_read_b128 v[68:71], v180 offset:57344
	ds_read_b128 v[200:203], v181 offset:49152
	ds_read_b128 v[226:229], v181 offset:57344
	ds_read_b128 v[230:233], v182 offset:49152
	ds_read_b128 v[234:237], v182 offset:57344
	ds_read_b128 v[238:241], v183 offset:49152
	ds_read_b128 v[242:245], v183 offset:57344
	s_waitcnt lgkmcnt(7)
	v_mfma_f32_32x32x16_bf16 v[80:95], v[64:67], v[124:127], 0
	s_add_i32 s8, s8, 2
	s_sub_i32 s80, s14, 64
	s_cmp_lt_u32 s8, 3
	s_cselect_b32 s80, s13, s80
	s_mul_i32 s81, s80, 0xc00
	s_add_i32 s85, s82, 0x8000
	s_mov_b32 m0, s85
	s_add_i32 s85, s82, 0x10000
	buffer_load_dwordx4 v154, s[72:75], s81 offen lds
	v_exp_f32_e32 v216, v128
	v_add_f32_e32 v128, 0, v222
	v_add_f32_e32 v128, v224, v128
	v_add_f32_e32 v128, v220, v128
	v_add_f32_e32 v128, v223, v128
	v_add_f32_e32 v128, v219, v128
	v_add_f32_e32 v128, v221, v128
	s_waitcnt lgkmcnt(6)
	v_mfma_f32_32x32x16_bf16 v[64:79], v[68:71], v[124:127], 0
	s_mov_b32 m0, s85
	s_add_i32 s85, s82, 0xa000
	buffer_load_dwordx4 v155, s[72:75], s81 offen lds
	v_add_f32_e32 v128, v217, v128
	v_add_f32_e32 v128, v218, v128
	v_add_f32_e32 v128, v212, v128
	v_add_f32_e32 v128, v214, v128
	v_add_f32_e32 v128, v211, v128
	v_add_f32_e32 v128, v213, v128
	v_exp_f32_e32 v138, v138
	s_waitcnt lgkmcnt(5)
	v_mfma_f32_32x32x16_bf16 v[80:95], v[200:203], v[120:123], v[80:95]
	s_mov_b32 m0, s85
	s_add_i32 s81, s81, 0x18000
	buffer_load_dwordx4 v154, s[72:75], s81 offen lds
	v_add_f32_e32 v128, v208, v128
	v_exp_f32_e32 v139, v139
	v_add_f32_e32 v128, v210, v128
	v_exp_f32_e32 v164, v136
	v_add_f32_e32 v128, v207, v128
	v_exp_f32_e32 v137, v137
	v_add_f32_e32 v128, v209, v128
	s_waitcnt lgkmcnt(4)
	v_mfma_f32_32x32x16_bf16 v[64:79], v[226:229], v[120:123], v[64:79]
	s_lshl_b32 s81, s83, 11
	s_add_i32 s85, s82, 0x4000
	s_mov_b32 m0, s85
	s_add_i32 s85, s82, 0x6000
	buffer_load_dwordx4 v158, s[76:79], s81 offen lds
	ds_read_b128 v[200:203], v184 offset:49152
	ds_read_b128 v[226:229], v184 offset:57344
	v_exp_f32_e32 v165, v132
	v_add_f32_e32 v128, v138, v128
	v_add_f32_e32 v128, v139, v128
	v_exp_f32_e32 v206, v130
	v_add_f32_e32 v128, v164, v128
	v_exp_f32_e32 v215, v131
	s_waitcnt lgkmcnt(5)
	v_mfma_f32_32x32x16_bf16 v[80:95], v[230:233], v[116:119], v[80:95]
	s_mov_b32 m0, s85
	s_add_i32 s81, s81, 0x10000
	buffer_load_dwordx4 v158, s[76:79], s81 offen lds
	s_mov_b32 s84, s80
	v_add_f32_e32 v128, v137, v128
	v_add_f32_e32 v128, v165, v128
	v_exp_f32_e32 v225, v129
	v_exp_f32_e32 v162, v162
	v_exp_f32_e32 v163, v163
	v_exp_f32_e32 v160, v160
	v_exp_f32_e32 v161, v161
	s_waitcnt lgkmcnt(4)
	v_mfma_f32_32x32x16_bf16 v[64:79], v[234:237], v[116:119], v[64:79]
	ds_read_b128 v[230:233], v185 offset:49152
	ds_read_b128 v[234:237], v185 offset:57344
	v_cvt_pk_bf16_f32 v129, v220, v223
	v_cvt_pk_bf16_f32 v130, v219, v221
	v_cvt_pk_bf16_f32 v131, v217, v218
	v_cvt_pk_bf16_f32 v132, v212, v214
	v_cvt_pk_bf16_f32 v136, v138, v139
	v_cvt_pk_bf16_f32 v137, v164, v137
	s_waitcnt lgkmcnt(5)
	v_mfma_f32_32x32x16_bf16 v[80:95], v[238:241], v[112:115], v[80:95]
	v_cvt_pk_bf16_f32 v139, v206, v215
	v_permlane32_swap_b32_e32 v129, v131
	s_nop 0
	v_permlane32_swap_b32_e32 v137, v139
	s_waitcnt lgkmcnt(4)
	v_mfma_f32_32x32x16_bf16 v[64:79], v[242:245], v[112:115], v[64:79]
	ds_read_b128 v[238:241], v186 offset:49152
	ds_read_b128 v[242:245], v186 offset:57344
	s_waitcnt lgkmcnt(5)
	v_mfma_f32_32x32x16_bf16 v[80:95], v[200:203], v[108:111], v[80:95]
	s_waitcnt lgkmcnt(4)
	v_mfma_f32_32x32x16_bf16 v[64:79], v[226:229], v[108:111], v[64:79]
	ds_read_b128 v[200:203], v187 offset:49152
	ds_read_b128 v[226:229], v187 offset:57344
	s_waitcnt lgkmcnt(5)
	v_mfma_f32_32x32x16_bf16 v[80:95], v[230:233], v[104:107], v[80:95]
	s_waitcnt lgkmcnt(4)
	v_mfma_f32_32x32x16_bf16 v[64:79], v[234:237], v[104:107], v[64:79]
	ds_read_b128 v[230:233], v199
	ds_read_b128 v[234:237], v199 offset:4096
	ds_read_b128 v[246:249], v190
	s_waitcnt lgkmcnt(6)
	v_mfma_f32_32x32x16_bf16 v[80:95], v[238:241], v[100:103], v[80:95]
	s_waitcnt lgkmcnt(5)
	v_mfma_f32_32x32x16_bf16 v[64:79], v[242:245], v[100:103], v[64:79]
	ds_read_b128 v[238:241], v204
	ds_read_b128 v[242:245], v204 offset:4096
	ds_read_b128 v[250:253], v190 offset:1024
	v_add_u32_e32 v204, s6, v173
	s_waitcnt lgkmcnt(7)
	v_mfma_f32_32x32x16_bf16 v[80:95], v[200:203], v[96:99], v[80:95]
	s_waitcnt lgkmcnt(6)
	v_mfma_f32_32x32x16_bf16 v[64:79], v[226:229], v[96:99], v[64:79]
	ds_read_b128 v[200:203], v205
	ds_read_b128 v[226:229], v205 offset:4096
	s_waitcnt lgkmcnt(5)
	v_mfma_f32_32x32x16_bf16 v[80:95], v[230:233], v[246:249], v[80:95]
	s_waitcnt lgkmcnt(5)
	v_mfma_f32_32x32x16_bf16 v[64:79], v[234:237], v[246:249], v[64:79]
	ds_read_b128 v[230:233], v204
	ds_read_b128 v[234:237], v204 offset:4096
	ds_read_b128 v[246:249], v190 offset:2048
	s_waitcnt lgkmcnt(5)
	v_mfma_f32_32x32x16_bf16 v[80:95], v[238:241], v[250:253], v[80:95]
	s_waitcnt lgkmcnt(5)
	v_mfma_f32_32x32x16_bf16 v[64:79], v[242:245], v[250:253], v[64:79]
	ds_read_b128 v[250:253], v190 offset:3072
	s_waitcnt lgkmcnt(1)
	v_mfma_f32_32x32x16_bf16 v[80:95], v[200:203], v[246:249], v[80:95]
	v_exp_f32_e32 v205, v133
	v_cvt_pk_bf16_f32 v133, v211, v213
	v_cvt_pk_bf16_f32 v138, v165, v205
	v_add_f32_e32 v128, v205, v128
	v_add_f32_e32 v128, v206, v128
	v_add_f32_e32 v128, v215, v128
	s_waitcnt lgkmcnt(1)
	v_mfma_f32_32x32x16_bf16 v[64:79], v[226:229], v[246:249], v[64:79]
	v_add_f32_e32 v128, v216, v128
	v_add_f32_e32 v128, v225, v128
	v_add_f32_e32 v128, v162, v128
	v_add_f32_e32 v128, v163, v128
	v_add_f32_e32 v128, v160, v128
	v_add_f32_e32 v128, v161, v128
	s_waitcnt lgkmcnt(0)
	v_mfma_f32_32x32x16_bf16 v[80:95], v[230:233], v[250:253], v[80:95]
	v_exp_f32_e32 v226, v134
	v_exp_f32_e32 v227, v135
	v_cvt_pk_bf16_f32 v134, v208, v210
	v_cvt_pk_bf16_f32 v135, v207, v209
	v_add_f32_e32 v128, v226, v128
	v_add_f32_e32 v203, v227, v128
	v_mov_b32_e32 v204, v203
	s_waitcnt lgkmcnt(0)
	v_mfma_f32_32x32x16_bf16 v[64:79], v[234:237], v[250:253], v[64:79]
	s_nop 0
	v_permlane32_swap_b32_e32 v203, v204
	v_cvt_pk_bf16_f32 v128, v222, v224
	v_cvt_pk_bf16_f32 v208, v216, v225
	v_cvt_pk_bf16_f32 v209, v162, v163
	v_cvt_pk_bf16_f32 v210, v160, v161
	v_cvt_pk_bf16_f32 v211, v226, v227
	v_permlane32_swap_b32_e32 v132, v134
	v_permlane32_swap_b32_e32 v128, v130
	v_permlane32_swap_b32_e32 v133, v135
	v_permlane32_swap_b32_e32 v136, v138
	v_permlane32_swap_b32_e32 v208, v210
	v_permlane32_swap_b32_e32 v209, v211
	ds_read_b64_tr_b16 v[160:161], v167 offset:0
	ds_read_b64_tr_b16 v[162:163], v167 offset:0x800
	ds_read_b64_tr_b16 v[232:233], v167 offset:0x1000
	ds_read_b64_tr_b16 v[234:235], v167 offset:0x1800
	ds_read_b64_tr_b16 v[236:237], v167 offset:0x2000
	ds_read_b64_tr_b16 v[238:239], v167 offset:0x2800
	ds_read_b64_tr_b16 v[240:241], v167 offset:0x3000
	ds_read_b64_tr_b16 v[242:243], v167 offset:0x3800
	v_max_f32_e32 v164, v81, v81
	v_max_f32_e32 v165, v80, v80
	v_max_f32_e32 v164, v165, v164
	v_max3_f32 v164, v164, v82, v83
	v_max3_f32 v164, v164, v84, v85
	v_max3_f32 v164, v164, v86, v87
	v_max3_f32 v164, v164, v88, v89
	v_max3_f32 v164, v164, v90, v91
	v_max3_f32 v164, v164, v92, v93
	v_max3_f32 v164, v164, v94, v95
	s_waitcnt lgkmcnt(0)
	v_mfma_f32_32x32x16_bf16 v[0:15], v[128:131], v[160:163], v[0:15]
	v_max3_f32 v160, v164, v64, v65
	v_max3_f32 v160, v160, v66, v67
	v_max3_f32 v160, v160, v68, v69
	v_mfma_f32_32x32x16_bf16 v[0:15], v[132:135], v[232:235], v[0:15]
	ds_read_b64_tr_b16 v[232:233], v167 offset:0x200
	ds_read_b64_tr_b16 v[234:235], v167 offset:0xa00
	v_max3_f32 v160, v160, v70, v71
	v_max3_f32 v160, v160, v72, v73
	v_max3_f32 v160, v160, v74, v75
	v_mfma_f32_32x32x16_bf16 v[0:15], v[136:139], v[236:239], v[0:15]
	ds_read_b64_tr_b16 v[236:237], v167 offset:0x1200
	ds_read_b64_tr_b16 v[238:239], v167 offset:0x1a00
	ds_read_b64_tr_b16 v[244:245], v167 offset:0x2200
	ds_read_b64_tr_b16 v[246:247], v167 offset:0x2a00
	ds_read_b64_tr_b16 v[248:249], v167 offset:0x3200
	ds_read_b64_tr_b16 v[250:251], v167 offset:0x3a00
	v_max3_f32 v160, v160, v76, v77
	v_max3_f32 v160, v160, v78, v79
	v_mov_b32_e32 v161, v160
	v_mfma_f32_32x32x16_bf16 v[0:15], v[208:211], v[240:243], v[0:15]
	v_max_f32_e32 v162, v198, v198
	v_permlane32_swap_b32_e32 v160, v161
	v_max_f32_e32 v161, v161, v161
	v_max_f32_e32 v160, v160, v160
	v_max_f32_e32 v160, v160, v161
	s_waitcnt lgkmcnt(0)
	v_mfma_f32_32x32x16_bf16 v[32:47], v[128:131], v[232:235], v[32:47]
	ds_read_b64_tr_b16 v[232:233], v167 offset:0x400
	ds_read_b64_tr_b16 v[234:235], v167 offset:0xc00
	v_sub_f32_e32 v161, v160, v198
	v_max_f32_e32 v160, v162, v160
	v_sub_f32_e32 v162, v198, v160
	v_mul_f32_e32 v162, 0x3dd53b94, v162
	v_exp_f32_e32 v162, v162
	v_mfma_f32_32x32x16_bf16 v[32:47], v[132:135], v[236:239], v[32:47]
	ds_read_b64_tr_b16 v[236:237], v167 offset:0x1400
	ds_read_b64_tr_b16 v[238:239], v167 offset:0x1c00
	ds_read_b64_tr_b16 v[240:241], v167 offset:0x2400
	ds_read_b64_tr_b16 v[242:243], v167 offset:0x2c00
	v_cmp_ge_f32_e32 vcc, s46, v161
	s_cmp_eq_u64 vcc, exec
	s_cselect_b64 s[6:7], -1, 0
	v_cndmask_b32_e64 v206, v162, 1.0, s[6:7]
	v_cndmask_b32_e64 v160, v160, v198, s[6:7]
	v_mul_f32_e32 v205, 0xbdd53b94, v160
	v_cmp_gt_f32_e32 vcc, 1.0, v206
	v_mfma_f32_32x32x16_bf16 v[32:47], v[136:139], v[244:247], v[32:47]
	ds_read_b64_tr_b16 v[244:245], v167 offset:0x3400
	ds_read_b64_tr_b16 v[246:247], v167 offset:0x3c00
	v_fmamk_f32 v87, v87, 0x3dd53b94, v205
	v_fmamk_f32 v80, v80, 0x3dd53b94, v205
	v_fmamk_f32 v81, v81, 0x3dd53b94, v205
	v_fmamk_f32 v82, v82, 0x3dd53b94, v205
	v_fmamk_f32 v83, v83, 0x3dd53b94, v205
	v_mfma_f32_32x32x16_bf16 v[32:47], v[208:211], v[248:251], v[32:47]
	v_fmamk_f32 v84, v84, 0x3dd53b94, v205
	v_fmamk_f32 v85, v85, 0x3dd53b94, v205
	v_fmamk_f32 v86, v86, 0x3dd53b94, v205
	v_fmamk_f32 v88, v88, 0x3dd53b94, v205
	v_fmamk_f32 v89, v89, 0x3dd53b94, v205
	s_waitcnt lgkmcnt(0)
	v_mfma_f32_32x32x16_bf16 v[16:31], v[128:131], v[232:235], v[16:31]
	ds_read_b64_tr_b16 v[232:233], v167 offset:0x600
	ds_read_b64_tr_b16 v[234:235], v167 offset:0xe00
	v_fmamk_f32 v90, v90, 0x3dd53b94, v205
	v_fmamk_f32 v91, v91, 0x3dd53b94, v205
	v_fmamk_f32 v92, v92, 0x3dd53b94, v205
	v_fmamk_f32 v93, v93, 0x3dd53b94, v205
	v_fmamk_f32 v94, v94, 0x3dd53b94, v205
	v_mfma_f32_32x32x16_bf16 v[16:31], v[132:135], v[236:239], v[16:31]
	ds_read_b64_tr_b16 v[236:237], v167 offset:0x1600
	ds_read_b64_tr_b16 v[238:239], v167 offset:0x1e00
	v_fmamk_f32 v95, v95, 0x3dd53b94, v205
	v_fmamk_f32 v215, v64, 0x3dd53b94, v205
	v_fmamk_f32 v216, v65, 0x3dd53b94, v205
	v_fmamk_f32 v217, v66, 0x3dd53b94, v205
	v_fmamk_f32 v218, v67, 0x3dd53b94, v205
	v_mfma_f32_32x32x16_bf16 v[16:31], v[136:139], v[240:243], v[16:31]
	ds_read_b64_tr_b16 v[240:241], v167 offset:0x2600
	ds_read_b64_tr_b16 v[242:243], v167 offset:0x2e00
	ds_read_b64_tr_b16 v[248:249], v167 offset:0x3600
	ds_read_b64_tr_b16 v[250:251], v167 offset:0x3e00
	v_fmamk_f32 v219, v68, 0x3dd53b94, v205
	v_fmamk_f32 v212, v73, 0x3dd53b94, v205
	v_fmamk_f32 v213, v74, 0x3dd53b94, v205
	v_fmamk_f32 v214, v75, 0x3dd53b94, v205
	v_mfma_f32_32x32x16_bf16 v[16:31], v[208:211], v[244:247], v[16:31]
	v_fmamk_f32 v207, v76, 0x3dd53b94, v205
	v_fmamk_f32 v220, v77, 0x3dd53b94, v205
	v_fmamk_f32 v221, v78, 0x3dd53b94, v205
	s_waitcnt lgkmcnt(0)
	v_mfma_f32_32x32x16_bf16 v[48:63], v[128:131], v[232:235], v[48:63]
	v_exp_f32_e32 v128, v80
	v_exp_f32_e32 v129, v82
	v_exp_f32_e32 v130, v84
	v_exp_f32_e32 v131, v86
	v_mfma_f32_32x32x16_bf16 v[48:63], v[132:135], v[236:239], v[48:63]
	v_exp_f32_e32 v132, v88
	v_exp_f32_e32 v133, v90
	v_exp_f32_e32 v134, v92
	v_exp_f32_e32 v135, v94
	v_mfma_f32_32x32x16_bf16 v[48:63], v[136:139], v[240:243], v[48:63]
	v_exp_f32_e32 v139, v89
	v_exp_f32_e32 v138, v91
	v_exp_f32_e32 v137, v93
	v_exp_f32_e32 v136, v95
	v_mfma_f32_32x32x16_bf16 v[48:63], v[208:211], v[248:251], v[48:63]
	v_exp_f32_e32 v161, v87
	v_exp_f32_e32 v198, v81
	v_exp_f32_e32 v163, v83
	v_exp_f32_e32 v162, v85
	v_fmamk_f32 v208, v69, 0x3dd53b94, v205
	v_fmamk_f32 v209, v70, 0x3dd53b94, v205
	v_fmamk_f32 v210, v71, 0x3dd53b94, v205
	v_fmamk_f32 v211, v72, 0x3dd53b94, v205
	v_fmac_f32_e32 v205, 0x3dd53b94, v79
	s_cbranch_vccz .LBB0_2016
	s_and_saveexec_b64 s[10:11], s[4:5]
	ds_write_b32 v189, v206 offset:128
	s_or_b64 exec, exec, s[10:11]
	s_waitcnt lgkmcnt(0)
	v_add_u32_e32 v248, s12, v169
	ds_read_b128 v[232:235], v248 offset:224
	ds_read_b128 v[236:239], v248 offset:192
	ds_read_b128 v[240:243], v248 offset:160
	ds_read_b128 v[244:247], v248 offset:128
	s_waitcnt lgkmcnt(3)
	v_pk_mul_f32 v[12:13], v[12:13], v[232:233]
	s_waitcnt lgkmcnt(2)
	v_pk_mul_f32 v[8:9], v[8:9], v[236:237]
	s_waitcnt lgkmcnt(1)
	v_pk_mul_f32 v[4:5], v[4:5], v[240:241]
	v_pk_mul_f32 v[14:15], v[14:15], v[234:235]
	v_pk_mul_f32 v[10:11], v[10:11], v[238:239]
	v_pk_mul_f32 v[6:7], v[6:7], v[242:243]
	s_waitcnt lgkmcnt(0)
	v_pk_mul_f32 v[2:3], v[2:3], v[246:247]
	v_pk_mul_f32 v[0:1], v[0:1], v[244:245]
	v_pk_mul_f32 v[44:45], v[44:45], v[232:233]
	v_pk_mul_f32 v[40:41], v[40:41], v[236:237]
	v_pk_mul_f32 v[36:37], v[36:37], v[240:241]
	v_pk_mul_f32 v[46:47], v[46:47], v[234:235]
	v_pk_mul_f32 v[42:43], v[42:43], v[238:239]
	v_pk_mul_f32 v[38:39], v[38:39], v[242:243]
	v_pk_mul_f32 v[34:35], v[34:35], v[246:247]
	v_pk_mul_f32 v[32:33], v[32:33], v[244:245]
	v_pk_mul_f32 v[28:29], v[28:29], v[232:233]
	v_pk_mul_f32 v[24:25], v[24:25], v[236:237]
	v_pk_mul_f32 v[20:21], v[20:21], v[240:241]
	v_pk_mul_f32 v[30:31], v[30:31], v[234:235]
	v_pk_mul_f32 v[26:27], v[26:27], v[238:239]
	v_pk_mul_f32 v[22:23], v[22:23], v[242:243]
	v_pk_mul_f32 v[18:19], v[18:19], v[246:247]
	v_pk_mul_f32 v[16:17], v[16:17], v[244:245]
	v_pk_mul_f32 v[60:61], v[60:61], v[232:233]
	v_pk_mul_f32 v[56:57], v[56:57], v[236:237]
	v_pk_mul_f32 v[52:53], v[52:53], v[240:241]
	v_pk_mul_f32 v[62:63], v[62:63], v[234:235]
	v_pk_mul_f32 v[58:59], v[58:59], v[238:239]
	v_pk_mul_f32 v[54:55], v[54:55], v[242:243]
	v_pk_mul_f32 v[50:51], v[50:51], v[246:247]
	v_pk_mul_f32 v[48:49], v[48:49], v[244:245]

.LBB0_2020:
	s_cmp_gt_u32 s8, 64
	s_waitcnt vmcnt(0) lgkmcnt(0)
	s_cbranch_scc1 .Lattn_exit_0
	v_mov_b32_e32 v197, v205
	s_branch .LBB0_2012
